# static s_setprio 1 for waves 4-7 extended to prologue, NORM1, odd mixer, MIXC, expert-weight conversion, NORM2 and the final norm
# baseline (speedup 1.0000x reference)
_Z10fwd_kernel4Args:
	v_readfirstlane_b32 s32, v0
	s_nop 3
	s_lshr_b32 s32, s32, 6
	s_cmp_ge_u32 s32, 4
	s_cbranch_scc0 .Lprio_x0
	s_setprio 1
.Lprio_x0:
	s_mov_b32 s84, s2
	s_add_u32 s2, s0, 0x140
	s_addc_u32 s3, s1, 0
	v_lshl_add_u32 v1, v0, 2, 0
	v_writelane_b32 v254, s2, 0
	v_add_u32_e32 v1, 0x23800, v1
	v_mov_b32_e32 v2, 0
	v_writelane_b32 v254, s3, 1
	s_load_dwordx2 s[2:3], s[0:1], 0x128
	s_waitcnt lgkmcnt(0)
	v_writelane_b32 v254, s2, 2
	s_nop 1
	v_writelane_b32 v254, s3, 3
	v_writelane_b32 v254, s0, 4
	s_load_dword s68, s[0:1], 0x140
	s_mov_b64 s[2:3], 0
	v_writelane_b32 v254, s1, 5
	s_mov_b32 s0, 0
	s_mov_b32 s1, 1
	s_mov_b32 s4, s0
	s_branch .LBB0_2

.LBB0_185:
	v_readfirstlane_b32 s32, v0
	s_nop 3
	s_lshr_b32 s32, s32, 6
	s_cmp_ge_u32 s32, 4
	s_cbranch_scc0 .Lprio_x1
	s_setprio 1
